# baseline (speedup 1.0000x reference)
.LBB3_6:
	v_lshlrev_b32_e32 v104, 3, v24
	v_or_b32_e32 v24, s18, v30
	v_mov_b32_e32 v25, s19
	v_lshlrev_b64 v[24:25], 12, v[24:25]
	v_lshl_add_u64 v[80:81], s[14:15], 0, v[24:25]
	v_lshrrev_b32_e32 v106, 2, v203
	v_lshlrev_b32_e32 v24, 1, v204
	v_bfe_u32 v25, v203, 2, 2
	s_and_b32 s7, s33, 3
	s_lshl_b32 s7, s7, 13
	s_lshr_b32 s62, s33, 2
	s_lshl_b32 s62, s62, 16
	s_mov_b32 s63, 0
	s_lshr_b32 s64, s33, 2
	s_lshl_b32 s64, s64, 12
	s_add_i32 s65, s64, 0x8000
	v_bitop3_b32 v26, v24, v106, 3 bitop3:0x78
	v_bitop3_b32 v24, v24, v25, 1 bitop3:0x36
	s_cmp_lg_u32 0, -1
	v_lshlrev_b32_e32 v218, 4, v24
	v_bitop3_b32 v24, v30, v0, 15 bitop3:0x78
	s_cselect_b32 s0, 0, 0
	v_lshlrev_b32_e32 v28, 4, v24
	s_add_i32 s23, s0, s7
	v_lshl_add_u64 v[164:165], v[80:81], 0, v[28:29]
	s_mov_b64 s[0:1], 0x0
	v_and_b32_e32 v105, 15, v0
	v_lshl_add_u64 v[24:25], v[164:165], 0, s[0:1]
	v_lshl_add_u64 v[24:25], v[24:25], 0, s[62:63]
	s_add_i32 s36, s23, 0x14800
	s_add_i32 m0, s36, s64
	s_nop 0
	global_load_lds_dwordx4 v[24:25], off nt
	v_bitop3_b32 v24, v30, v105, 4 bitop3:0x36
	v_lshlrev_b32_e32 v28, 4, v24
	v_lshl_add_u64 v[24:25], v[80:81], 0, v[28:29]
	s_mov_b64 s[8:9], 0x4000
	v_lshlrev_b32_e32 v217, 4, v26
	v_lshl_add_u64 v[26:27], v[24:25], 0, s[8:9]
	v_lshl_add_u64 v[26:27], v[26:27], 0, s[62:63]
	s_add_i32 s8, s23, 0x14c00
	s_add_i32 m0, s8, s64
	s_nop 0
	global_load_lds_dwordx4 v[26:27], off nt
	v_bitop3_b32 v26, v30, v105, 8 bitop3:0x36
	v_lshlrev_b32_e32 v28, 4, v26
	v_lshl_add_u64 v[26:27], v[80:81], 0, v[28:29]
	s_mov_b64 s[14:15], 0x8000
	v_bitop3_b32 v28, v30, v105, 12 bitop3:0x36
	v_lshl_add_u64 v[82:83], v[26:27], 0, s[14:15]
	v_lshl_add_u64 v[82:83], v[82:83], 0, s[62:63]
	s_add_i32 s14, s23, 0x15000
	s_add_i32 m0, s14, s64
	s_nop 0
	global_load_lds_dwordx4 v[82:83], off nt
	v_lshlrev_b32_e32 v28, 4, v28
	v_lshl_add_u64 v[28:29], v[80:81], 0, v[28:29]
	s_mov_b64 s[14:15], 0xc000
	v_lshl_add_u64 v[80:81], v[28:29], 0, s[14:15]
	v_lshl_add_u64 v[80:81], v[80:81], 0, s[62:63]
	s_add_i32 s14, s23, 0x15400
	s_add_i32 m0, s14, s64
	s_nop 0
	global_load_lds_dwordx4 v[80:81], off nt
	s_mov_b64 s[26:27], 0x10000
	s_add_i32 s26, s23, 0x15800
	s_mov_b64 s[28:29], 0x14000
	s_add_i32 s28, s23, 0x15c00
	s_mov_b64 s[30:31], 0x18000
	s_add_i32 s30, s23, 0x16000
	s_mov_b64 s[30:31], 0x1c000
	v_lshl_add_u32 v216, v203, 6, 0
	v_add_u32_e32 v216, s57, v216
	s_add_i32 s23, s23, 0x16400
	s_mov_b64 s[52:53], 0x100
	v_lshl_add_u64 v[224:225], v[164:165], 0, s[52:53]
	v_lshl_add_u64 v[224:225], v[224:225], 0, s[62:63]
	s_add_i32 s54, s36, 0x0
	s_add_i32 m0, s54, s65
	s_nop 0
	global_load_lds_dwordx4 v[224:225], off nt
	s_mov_b64 s[52:53], 0x4100
	v_lshl_add_u64 v[224:225], v[24:25], 0, s[52:53]
	v_lshl_add_u64 v[224:225], v[224:225], 0, s[62:63]
	s_add_i32 s54, s36, 0x400
	s_add_i32 m0, s54, s65
	s_nop 0
	global_load_lds_dwordx4 v[224:225], off nt
	s_mov_b64 s[52:53], 0x8100
	v_lshl_add_u64 v[224:225], v[26:27], 0, s[52:53]
	v_lshl_add_u64 v[224:225], v[224:225], 0, s[62:63]
	s_add_i32 s54, s36, 0x800
	s_add_i32 m0, s54, s65
	s_nop 0
	global_load_lds_dwordx4 v[224:225], off nt
	s_mov_b64 s[52:53], 0xc100
	v_lshl_add_u64 v[224:225], v[28:29], 0, s[52:53]
	v_lshl_add_u64 v[224:225], v[224:225], 0, s[62:63]
	s_add_i32 s54, s36, 0xc00
	s_add_i32 m0, s54, s65
	s_nop 0
	global_load_lds_dwordx4 v[224:225], off nt
	s_waitcnt vmcnt(0) lgkmcnt(0)
	s_barrier
	v_and_b32_e32 v226, 31, v0
	v_bfe_u32 v227, v0, 5, 1
	v_lshrrev_b32_e32 v228, 2, v226
	v_lshlrev_b32_e32 v228, 10, v228
	v_and_b32_e32 v229, 3, v226
	v_lshlrev_b32_e32 v229, 8, v229
	v_add3_u32 v230, s36, v228, v229
	v_and_b32_e32 v231, 15, v226
	v_xor_b32_e32 v231, v231, v227
	v_lshlrev_b32_e32 v231, 4, v231
	v_mov_b32_e32 v232, v231
	v_add_u32_e32 v232, v230, v232
	ds_read_b128 v[64:67], v232
	v_xor_b32_e32 v233, 0x80, v231
	v_add_u32_e32 v233, v230, v233
	ds_read_b128 v[2:5], v233
	v_xor_b32_e32 v234, 0x20, v231
	v_add_u32_e32 v234, v230, v234
	ds_read_b128 v[68:71], v234
	v_xor_b32_e32 v235, 0xa0, v231
	v_add_u32_e32 v235, v230, v235
	ds_read_b128 v[6:9], v235
	v_xor_b32_e32 v236, 0x40, v231
	v_add_u32_e32 v236, v230, v236
	ds_read_b128 v[72:75], v236
	v_xor_b32_e32 v237, 0xc0, v231
	v_add_u32_e32 v237, v230, v237
	ds_read_b128 v[10:13], v237
	v_xor_b32_e32 v238, 0x60, v231
	v_add_u32_e32 v238, v230, v238
	ds_read_b128 v[76:79], v238
	v_xor_b32_e32 v239, 0xe0, v231
	v_add_u32_e32 v239, v230, v239
	ds_read_b128 v[14:17], v239
	s_waitcnt lgkmcnt(0)
	s_mov_b64 s[52:53], 0x10100
	s_add_i32 s54, s36, 0x1000
	s_mov_b64 s[52:53], 0x14100
	s_add_i32 s54, s36, 0x1400
	s_mov_b64 s[52:53], 0x18100
	s_add_i32 s54, s36, 0x1800
	s_mov_b64 s[52:53], 0x1c100
	s_add_i32 s54, s36, 0x1c00
	v_add_u32_e32 v209, v216, v217
	v_add_u32_e32 v210, v216, v218
	ds_read_b128 v[80:83], v209
	ds_read_b128 v[88:91], v209 offset:2048
	ds_read_b128 v[84:87], v210
	ds_read_b128 v[92:95], v210 offset:2048
	v_mov_b32_e32 v219, 0x7f7f7f7f
	v_mov_b32_e32 v220, 0x7c7c7c7c
	s_waitcnt vmcnt(10) lgkmcnt(1)
	v_mfma_scale_f32_32x32x64_f8f6f4 v[64:79], v[80:87], v[96:103], v[64:79], v219, v220 op_sel_hi:[0,0,0]
	s_waitcnt vmcnt(8) lgkmcnt(0)
	v_mfma_scale_f32_32x32x64_f8f6f4 v[2:17], v[88:95], v[96:103], v[2:17], v219, v220 op_sel_hi:[0,0,0]
	s_mov_b32 s39, 0x3fb8aa3b
	s_nop 15
	s_nop 15
	s_nop 15
	s_nop 15
	s_nop 15
	s_nop 15
	s_waitcnt vmcnt(0) lgkmcnt(0)
	s_barrier
	ds_read_b128 v[48:51], v232 offset:32768
	ds_read_b128 v[32:35], v233 offset:32768
	ds_read_b128 v[52:55], v234 offset:32768
	ds_read_b128 v[36:39], v235 offset:32768
	ds_read_b128 v[56:59], v236 offset:32768
	ds_read_b128 v[40:43], v237 offset:32768
	ds_read_b128 v[60:63], v238 offset:32768
	ds_read_b128 v[44:47], v239 offset:32768
	s_waitcnt lgkmcnt(0)
	s_mov_b64 s[52:53], 0x200
	v_lshl_add_u64 v[224:225], v[164:165], 0, s[52:53]
	v_lshl_add_u64 v[224:225], v[224:225], 0, s[62:63]
	s_add_i32 s54, s36, 0x0
	s_add_i32 m0, s54, s64
	s_nop 0
	global_load_lds_dwordx4 v[224:225], off nt
	s_mov_b64 s[52:53], 0x4200
	v_lshl_add_u64 v[224:225], v[24:25], 0, s[52:53]
	v_lshl_add_u64 v[224:225], v[224:225], 0, s[62:63]
	s_add_i32 s54, s36, 0x400
	s_add_i32 m0, s54, s64
	s_nop 0
	global_load_lds_dwordx4 v[224:225], off nt
	s_mov_b64 s[52:53], 0x8200
	v_lshl_add_u64 v[224:225], v[26:27], 0, s[52:53]
	v_lshl_add_u64 v[224:225], v[224:225], 0, s[62:63]
	s_add_i32 s54, s36, 0x800
	s_add_i32 m0, s54, s64
	s_nop 0
	global_load_lds_dwordx4 v[224:225], off nt
	s_mov_b64 s[52:53], 0xc200
	v_lshl_add_u64 v[224:225], v[28:29], 0, s[52:53]
	v_lshl_add_u64 v[224:225], v[224:225], 0, s[62:63]
	s_add_i32 s54, s36, 0xc00
	s_add_i32 m0, s54, s64
	s_nop 0
	global_load_lds_dwordx4 v[224:225], off nt
	v_lshlrev_b32_e32 v31, 2, v204
	v_max_f32_e32 v80, v65, v65
	v_max_f32_e32 v81, v64, v64
	v_max_f32_e32 v80, v81, v80
	v_max3_f32 v81, v66, v67, v3
	v_max3_f32 v80, v80, v2, v4
	v_max3_f32 v80, v80, v5, v68
	v_max3_f32 v81, v81, v70, v71
	v_max3_f32 v80, v80, v69, v6
	v_max3_f32 v81, v81, v8, v9
	v_max3_f32 v80, v80, v7, v72
	v_max3_f32 v81, v81, v74, v75
	v_max3_f32 v80, v80, v73, v10
	v_max3_f32 v81, v81, v12, v13
	v_max3_f32 v80, v80, v11, v76
	v_max3_f32 v81, v81, v78, v79
	v_max3_f32 v80, v80, v77, v14
	v_max3_f32 v81, v81, v16, v17
	v_max3_f32 v80, v80, v15, v81
	v_mov_b32_e32 v81, v80
	s_nop 1
	v_permlane32_swap_b32_e32 v80, v81
	v_max_f32_e32 v81, v81, v81
	v_max_f32_e32 v80, v80, v80
	v_max_f32_e32 v80, v80, v81
	v_mul_f32_e32 v208, 0x3fb8aa3b, v80
	s_mov_b32 s48, 0
	s_mov_b32 s38, -1
	s_mov_b64 s[0:1], 0x4000
	s_mov_b64 s[8:9], 0x8000
	s_mov_b64 s[24:25], 0xc000
	s_mov_b64 s[14:15], 0x10000
	s_mov_b64 s[26:27], 0x14000
	s_mov_b64 s[28:29], 0x18000
	s_mov_b64 s[30:31], 0x1c000
	v_fma_f32 v64, v64, s39, -v208
	v_fma_f32 v2, v2, s39, -v208
	v_fma_f32 v65, v65, s39, -v208
	v_fma_f32 v3, v3, s39, -v208
	v_fma_f32 v66, v66, s39, -v208
	v_fma_f32 v4, v4, s39, -v208
	v_fma_f32 v67, v67, s39, -v208
	v_fma_f32 v5, v5, s39, -v208
	v_fma_f32 v68, v68, s39, -v208
	v_fma_f32 v6, v6, s39, -v208
	v_fma_f32 v69, v69, s39, -v208
	v_fma_f32 v7, v7, s39, -v208
	v_fma_f32 v70, v70, s39, -v208
	v_fma_f32 v8, v8, s39, -v208
	v_fma_f32 v71, v71, s39, -v208
	v_fma_f32 v9, v9, s39, -v208
	v_fma_f32 v72, v72, s39, -v208
	v_fma_f32 v10, v10, s39, -v208
	v_fma_f32 v73, v73, s39, -v208
	v_fma_f32 v11, v11, s39, -v208
	v_fma_f32 v74, v74, s39, -v208
	v_fma_f32 v12, v12, s39, -v208
	v_fma_f32 v75, v75, s39, -v208
	v_fma_f32 v13, v13, s39, -v208
	v_fma_f32 v76, v76, s39, -v208
	v_fma_f32 v14, v14, s39, -v208
	v_fma_f32 v77, v77, s39, -v208
	v_fma_f32 v78, v78, s39, -v208
	v_fma_f32 v79, v79, s39, -v208
	v_fma_f32 v94, v15, s39, -v208
	v_fma_f32 v16, v16, s39, -v208
	v_fma_f32 v15, v17, s39, -v208
	s_and_b64 vcc, exec, s[4:5]
	s_nop 0
	s_mov_b64 s[42:43], 0x30000
	v_lshl_add_u64 v[22:23], v[22:23], 0, s[42:43]
	s_mov_b32 m0, s37
	s_nop 0
	global_load_lds_dwordx4 v[22:23], off

.LBB6_6:
	v_lshlrev_b32_e32 v30, 3, v22
	v_or_b32_e32 v22, s18, v28
	v_mov_b32_e32 v23, s19
	v_lshlrev_b64 v[22:23], 13, v[22:23]
	v_lshl_add_u64 v[80:81], s[14:15], 0, v[22:23]
	v_lshrrev_b32_e32 v104, 2, v203
	v_lshlrev_b32_e32 v22, 1, v204
	v_bfe_u32 v23, v203, 2, 2
	s_and_b32 s7, s33, 3
	s_lshl_b32 s7, s7, 13
	s_lshr_b32 s62, s33, 2
	s_lshl_b32 s62, s62, 17
	s_mov_b32 s63, 0
	s_lshr_b32 s64, s33, 2
	s_lshl_b32 s64, s64, 12
	s_add_i32 s65, s64, 0x8000
	v_bitop3_b32 v24, v22, v104, 3 bitop3:0x78
	v_bitop3_b32 v22, v22, v23, 1 bitop3:0x36
	s_cmp_lg_u32 0, -1
	v_lshlrev_b32_e32 v218, 4, v22
	v_bitop3_b32 v22, v28, v0, 15 bitop3:0x78
	s_cselect_b32 s0, 0, 0
	v_lshlrev_b32_e32 v26, 4, v22
	s_add_i32 s41, s0, s7
	v_lshl_add_u64 v[164:165], v[80:81], 0, v[26:27]
	s_mov_b64 s[0:1], 0x0
	v_and_b32_e32 v31, 15, v0
	v_lshl_add_u64 v[22:23], v[164:165], 0, s[0:1]
	v_lshl_add_u64 v[22:23], v[22:23], 0, s[62:63]
	s_add_i32 s38, s41, 0x14800
	s_add_i32 m0, s38, s64
	s_nop 0
	global_load_lds_dwordx4 v[22:23], off nt
	v_bitop3_b32 v22, v28, v31, 4 bitop3:0x36
	v_lshlrev_b32_e32 v26, 4, v22
	v_lshl_add_u64 v[22:23], v[80:81], 0, v[26:27]
	s_mov_b64 s[8:9], 0x8000
	v_lshlrev_b32_e32 v217, 4, v24
	v_lshl_add_u64 v[24:25], v[22:23], 0, s[8:9]
	v_lshl_add_u64 v[24:25], v[24:25], 0, s[62:63]
	s_add_i32 s8, s41, 0x14c00
	s_add_i32 m0, s8, s64
	s_nop 0
	global_load_lds_dwordx4 v[24:25], off nt
	v_bitop3_b32 v24, v28, v31, 8 bitop3:0x36
	v_lshlrev_b32_e32 v26, 4, v24
	v_lshl_add_u64 v[24:25], v[80:81], 0, v[26:27]
	s_mov_b64 s[8:9], 0x10000
	v_bitop3_b32 v26, v28, v31, 12 bitop3:0x36
	v_lshl_add_u64 v[82:83], v[24:25], 0, s[8:9]
	v_lshl_add_u64 v[82:83], v[82:83], 0, s[62:63]
	s_add_i32 s8, s41, 0x15000
	s_add_i32 m0, s8, s64
	s_nop 0
	global_load_lds_dwordx4 v[82:83], off nt
	v_lshlrev_b32_e32 v26, 4, v26
	v_lshl_add_u64 v[26:27], v[80:81], 0, v[26:27]
	s_mov_b64 s[8:9], 0x18000
	v_lshl_add_u64 v[80:81], v[26:27], 0, s[8:9]
	v_lshl_add_u64 v[80:81], v[80:81], 0, s[62:63]
	s_add_i32 s8, s41, 0x15400
	s_add_i32 m0, s8, s64
	s_nop 0
	global_load_lds_dwordx4 v[80:81], off nt
	s_mov_b64 s[14:15], 0x20000
	s_add_i32 s14, s41, 0x15800
	s_mov_b64 s[14:15], 0x28000
	s_add_i32 s14, s41, 0x15c00
	s_mov_b64 s[34:35], 0x30000
	s_add_i32 s34, s41, 0x16000
	s_mov_b64 s[34:35], 0x38000
	v_lshl_add_u32 v216, v203, 6, 0
	v_add_u32_e32 v216, s57, v216
	s_add_i32 s41, s41, 0x16400
	s_mov_b64 s[52:53], 0x100
	v_lshl_add_u64 v[224:225], v[164:165], 0, s[52:53]
	v_lshl_add_u64 v[224:225], v[224:225], 0, s[62:63]
	s_add_i32 s54, s38, 0x0
	s_add_i32 m0, s54, s65
	s_nop 0
	global_load_lds_dwordx4 v[224:225], off nt
	s_mov_b64 s[52:53], 0x8100
	v_lshl_add_u64 v[224:225], v[22:23], 0, s[52:53]
	v_lshl_add_u64 v[224:225], v[224:225], 0, s[62:63]
	s_add_i32 s54, s38, 0x400
	s_add_i32 m0, s54, s65
	s_nop 0
	global_load_lds_dwordx4 v[224:225], off nt
	s_mov_b64 s[52:53], 0x10100
	v_lshl_add_u64 v[224:225], v[24:25], 0, s[52:53]
	v_lshl_add_u64 v[224:225], v[224:225], 0, s[62:63]
	s_add_i32 s54, s38, 0x800
	s_add_i32 m0, s54, s65
	s_nop 0
	global_load_lds_dwordx4 v[224:225], off nt
	s_mov_b64 s[52:53], 0x18100
	v_lshl_add_u64 v[224:225], v[26:27], 0, s[52:53]
	v_lshl_add_u64 v[224:225], v[224:225], 0, s[62:63]
	s_add_i32 s54, s38, 0xc00
	s_add_i32 m0, s54, s65
	s_nop 0
	global_load_lds_dwordx4 v[224:225], off nt
	s_waitcnt vmcnt(0) lgkmcnt(0)
	s_barrier
	v_and_b32_e32 v226, 31, v0
	v_bfe_u32 v227, v0, 5, 1
	v_lshrrev_b32_e32 v228, 2, v226
	v_lshlrev_b32_e32 v228, 10, v228
	v_and_b32_e32 v229, 3, v226
	v_lshlrev_b32_e32 v229, 8, v229
	v_add3_u32 v230, s38, v228, v229
	v_and_b32_e32 v231, 15, v226
	v_xor_b32_e32 v231, v231, v227
	v_lshlrev_b32_e32 v231, 4, v231
	v_mov_b32_e32 v232, v231
	v_add_u32_e32 v232, v230, v232
	ds_read_b128 v[64:67], v232
	v_xor_b32_e32 v233, 0x80, v231
	v_add_u32_e32 v233, v230, v233
	ds_read_b128 v[2:5], v233
	v_xor_b32_e32 v234, 0x20, v231
	v_add_u32_e32 v234, v230, v234
	ds_read_b128 v[68:71], v234
	v_xor_b32_e32 v235, 0xa0, v231
	v_add_u32_e32 v235, v230, v235
	ds_read_b128 v[6:9], v235
	v_xor_b32_e32 v236, 0x40, v231
	v_add_u32_e32 v236, v230, v236
	ds_read_b128 v[72:75], v236
	v_xor_b32_e32 v237, 0xc0, v231
	v_add_u32_e32 v237, v230, v237
	ds_read_b128 v[10:13], v237
	v_xor_b32_e32 v238, 0x60, v231
	v_add_u32_e32 v238, v230, v238
	ds_read_b128 v[76:79], v238
	v_xor_b32_e32 v239, 0xe0, v231
	v_add_u32_e32 v239, v230, v239
	ds_read_b128 v[14:17], v239
	s_waitcnt lgkmcnt(0)
	s_mov_b64 s[52:53], 0x20100
	s_add_i32 s54, s38, 0x1000
	s_mov_b64 s[52:53], 0x28100
	s_add_i32 s54, s38, 0x1400
	s_mov_b64 s[52:53], 0x30100
	s_add_i32 s54, s38, 0x1800
	s_mov_b64 s[52:53], 0x38100
	s_add_i32 s54, s38, 0x1c00
	v_add_u32_e32 v209, v216, v217
	v_add_u32_e32 v210, v216, v218
	ds_read_b128 v[80:83], v209
	ds_read_b128 v[88:91], v209 offset:2048
	ds_read_b128 v[84:87], v210
	ds_read_b128 v[92:95], v210 offset:2048
	v_mov_b32_e32 v219, 0x7f7f7f7f
	v_mov_b32_e32 v220, 0x7c7c7c7c
	s_waitcnt vmcnt(10) lgkmcnt(1)
	v_mfma_scale_f32_32x32x64_f8f6f4 v[64:79], v[80:87], v[96:103], v[64:79], v219, v220 op_sel_hi:[0,0,0]
	s_waitcnt vmcnt(8) lgkmcnt(0)
	v_mfma_scale_f32_32x32x64_f8f6f4 v[2:17], v[88:95], v[96:103], v[2:17], v219, v220 op_sel_hi:[0,0,0]
	s_mov_b32 s41, 0x3fb8aa3b
	s_nop 15
	s_nop 15
	s_nop 15
	s_nop 15
	s_nop 15
	s_nop 15
	s_waitcnt vmcnt(0) lgkmcnt(0)
	s_barrier
	ds_read_b128 v[48:51], v232 offset:32768
	ds_read_b128 v[32:35], v233 offset:32768
	ds_read_b128 v[52:55], v234 offset:32768
	ds_read_b128 v[36:39], v235 offset:32768
	ds_read_b128 v[56:59], v236 offset:32768
	ds_read_b128 v[40:43], v237 offset:32768
	ds_read_b128 v[60:63], v238 offset:32768
	ds_read_b128 v[44:47], v239 offset:32768
	s_waitcnt lgkmcnt(0)
	s_mov_b64 s[52:53], 0x200
	v_lshl_add_u64 v[224:225], v[164:165], 0, s[52:53]
	v_lshl_add_u64 v[224:225], v[224:225], 0, s[62:63]
	s_add_i32 s54, s38, 0x0
	s_add_i32 m0, s54, s64
	s_nop 0
	global_load_lds_dwordx4 v[224:225], off nt
	s_mov_b64 s[52:53], 0x8200
	v_lshl_add_u64 v[224:225], v[22:23], 0, s[52:53]
	v_lshl_add_u64 v[224:225], v[224:225], 0, s[62:63]
	s_add_i32 s54, s38, 0x400
	s_add_i32 m0, s54, s64
	s_nop 0
	global_load_lds_dwordx4 v[224:225], off nt
	s_mov_b64 s[52:53], 0x10200
	v_lshl_add_u64 v[224:225], v[24:25], 0, s[52:53]
	v_lshl_add_u64 v[224:225], v[224:225], 0, s[62:63]
	s_add_i32 s54, s38, 0x800
	s_add_i32 m0, s54, s64
	s_nop 0
	global_load_lds_dwordx4 v[224:225], off nt
	s_mov_b64 s[52:53], 0x18200
	v_lshl_add_u64 v[224:225], v[26:27], 0, s[52:53]
	v_lshl_add_u64 v[224:225], v[224:225], 0, s[62:63]
	s_add_i32 s54, s38, 0xc00
	s_add_i32 m0, s54, s64
	s_nop 0
	global_load_lds_dwordx4 v[224:225], off nt
	v_lshlrev_b32_e32 v29, 2, v204
	v_max_f32_e32 v80, v65, v65
	v_max_f32_e32 v81, v64, v64
	v_max_f32_e32 v80, v81, v80
	v_max3_f32 v81, v66, v67, v3
	v_max3_f32 v80, v80, v2, v4
	v_max3_f32 v80, v80, v5, v68
	v_max3_f32 v81, v81, v70, v71
	v_max3_f32 v80, v80, v69, v6
	v_max3_f32 v81, v81, v8, v9
	v_max3_f32 v80, v80, v7, v72
	v_max3_f32 v81, v81, v74, v75
	v_max3_f32 v80, v80, v73, v10
	v_max3_f32 v81, v81, v12, v13
	v_max3_f32 v80, v80, v11, v76
	v_max3_f32 v81, v81, v78, v79
	v_max3_f32 v80, v80, v77, v14
	v_max3_f32 v81, v81, v16, v17
	v_max3_f32 v80, v80, v15, v81
	v_mov_b32_e32 v81, v80
	s_nop 1
	v_permlane32_swap_b32_e32 v80, v81
	v_max_f32_e32 v81, v81, v81
	v_max_f32_e32 v80, v80, v80
	v_max_f32_e32 v80, v80, v81
	v_mul_f32_e32 v208, 0x3fb8aa3b, v80
	s_mov_b32 s27, 0
	s_mov_b32 s40, -1
	s_mov_b64 s[0:1], 0x8000
	s_mov_b64 s[28:29], 0x10000
	s_mov_b64 s[20:21], 0x18000
	s_mov_b64 s[8:9], 0x20000
	s_mov_b64 s[30:31], 0x28000
	s_mov_b64 s[14:15], 0x30000
	s_mov_b64 s[34:35], 0x38000
	v_fma_f32 v64, v64, s41, -v208
	v_fma_f32 v2, v2, s41, -v208
	v_fma_f32 v65, v65, s41, -v208
	v_fma_f32 v3, v3, s41, -v208
	v_fma_f32 v66, v66, s41, -v208
	v_fma_f32 v4, v4, s41, -v208
	v_fma_f32 v67, v67, s41, -v208
	v_fma_f32 v5, v5, s41, -v208
	v_fma_f32 v68, v68, s41, -v208
	v_fma_f32 v6, v6, s41, -v208
	v_fma_f32 v69, v69, s41, -v208
	v_fma_f32 v7, v7, s41, -v208
	v_fma_f32 v70, v70, s41, -v208
	v_fma_f32 v8, v8, s41, -v208
	v_fma_f32 v71, v71, s41, -v208
	v_fma_f32 v9, v9, s41, -v208
	v_fma_f32 v72, v72, s41, -v208
	v_fma_f32 v10, v10, s41, -v208
	v_fma_f32 v73, v73, s41, -v208
	v_fma_f32 v11, v11, s41, -v208
	v_fma_f32 v74, v74, s41, -v208
	v_fma_f32 v12, v12, s41, -v208
	v_fma_f32 v75, v75, s41, -v208
	v_fma_f32 v13, v13, s41, -v208
	v_fma_f32 v76, v76, s41, -v208
	v_fma_f32 v14, v14, s41, -v208
	v_fma_f32 v77, v77, s41, -v208
	v_fma_f32 v78, v78, s41, -v208
	v_fma_f32 v79, v79, s41, -v208
	v_fma_f32 v94, v15, s41, -v208
	v_fma_f32 v16, v16, s41, -v208
	v_fma_f32 v15, v17, s41, -v208
	s_and_b64 vcc, exec, s[4:5]
	s_nop 0
	v_lshl_add_u64 v[20:21], v[20:21], 0, s[14:15]
	s_mov_b32 m0, s39
	s_nop 0
	global_load_lds_dwordx4 v[20:21], off
